# tail LDS reorder: next-node bias-init LDS reads moved behind the partial-sum write and the post-barrier partial reads; b2 scalar load moved to own step 0
# speedup vs baseline: 1.0075x; 1.0041x over previous
.LBB1_4:
	s_and_saveexec_b64 s[8:9], s[2:3]
	v_perm_b32 v5, v1, v102, s23
	v_perm_b32 v9, v121, v103, s23
	s_or_b64 exec, exec, s[8:9]
	v_mov_b32_e32 v144, v1
	v_mov_b32_e32 v145, v121
	v_mfma_f32_16x16x32_f16 v[164:167], v[30:33], v[2:5], 0
	v_mfma_f32_16x16x32_f16 v[180:183], v[22:25], v[2:5], 0
	s_cmp_lg_u32 s22, 0x818000
	v_permlane32_swap_b32_e32 v1, v144
	v_permlane32_swap_b32_e32 v121, v145
	v_mfma_f32_16x16x32_f16 v[168:171], v[30:33], v[6:9], 0
	v_mfma_f32_16x16x32_f16 v[184:187], v[22:25], v[6:9], 0
	s_cselect_b32 s9, s11, 15
	s_and_saveexec_b64 s[32:33], s[2:3]
	v_perm_b32 v17, v144, v115, s23
	v_perm_b32 v29, v145, v116, s23
	s_or_b64 exec, exec, s[32:33]
	v_mfma_f32_16x16x32_f16 v[172:175], v[30:33], v[14:17], 0
	v_mfma_f32_16x16x32_f16 v[188:191], v[22:25], v[14:17], 0
	v_mfma_f32_16x16x32_f16 v[176:179], v[30:33], v[26:29], 0
	v_mfma_f32_16x16x32_f16 v[192:195], v[22:25], v[26:29], 0
	v_mfma_f32_16x16x32_f16 v[208:211], v[18:21], v[2:5], 0
	v_mfma_f32_16x16x32_f16 v[224:227], v[10:13], v[2:5], 0
	v_cvt_pk_f16_f32 v122, v164, v165
	v_cvt_pk_f16_f32 v123, v166, v167
	v_pk_max_f16 v122, v122, 0
	v_pk_max_f16 v123, v123, 0
	v_cvt_pk_f16_f32 v124, v180, v181
	v_cvt_pk_f16_f32 v125, v182, v183
	v_pk_max_f16 v124, v124, 0
	v_pk_max_f16 v125, v125, 0
	ds_write_b128 v107, v[122:125]
	v_mfma_f32_16x16x32_f16 v[212:215], v[18:21], v[6:9], 0
	v_mfma_f32_16x16x32_f16 v[228:231], v[10:13], v[6:9], 0
	v_cvt_pk_f16_f32 v126, v168, v169
	v_cvt_pk_f16_f32 v127, v170, v171
	v_pk_max_f16 v126, v126, 0
	v_pk_max_f16 v127, v127, 0
	v_cvt_pk_f16_f32 v128, v184, v185
	v_cvt_pk_f16_f32 v129, v186, v187
	v_pk_max_f16 v128, v128, 0
	v_pk_max_f16 v129, v129, 0
	ds_write_b128 v107, v[126:129] offset:16384
	v_mfma_f32_16x16x32_f16 v[216:219], v[18:21], v[14:17], 0
	v_mfma_f32_16x16x32_f16 v[232:235], v[10:13], v[14:17], 0
	v_cvt_pk_f16_f32 v134, v172, v173
	v_cvt_pk_f16_f32 v135, v174, v175
	v_pk_max_f16 v134, v134, 0
	v_pk_max_f16 v135, v135, 0
	v_cvt_pk_f16_f32 v136, v188, v189
	v_cvt_pk_f16_f32 v137, v190, v191
	v_pk_max_f16 v136, v136, 0
	v_pk_max_f16 v137, v137, 0
	ds_write_b128 v107, v[134:137] offset:32768
	v_mfma_f32_16x16x32_f16 v[220:223], v[18:21], v[26:29], 0
	v_mfma_f32_16x16x32_f16 v[236:239], v[10:13], v[26:29], 0
	v_cvt_pk_f16_f32 v138, v176, v177
	v_cvt_pk_f16_f32 v139, v178, v179
	v_pk_max_f16 v138, v138, 0
	v_pk_max_f16 v139, v139, 0
	v_cvt_pk_f16_f32 v140, v192, v193
	v_cvt_pk_f16_f32 v141, v194, v195
	v_pk_max_f16 v140, v140, 0
	v_pk_max_f16 v141, v141, 0
	ds_write_b128 v107, v[138:141] offset:49152
	v_add_u32_e32 v111, s64, v111
	v_add_u32_e32 v98, s65, v98
	s_lshl_b32 s20, s9, 7
	v_lshl_add_u64 v[0:1], s[20:21], 3, v[132:133]
	s_add_i32 s25, s22, s34
	s_lshl_b32 s8, s9, 8
	buffer_load_dwordx4 v[192:195], v147, s[16:19], s25 offen
	buffer_load_dwordx4 v[196:199], v148, s[16:19], s25 offen
	buffer_load_dwordx4 v[200:203], v149, s[16:19], s25 offen
	buffer_load_dwordx4 v[204:207], v150, s[16:19], s25 offen
	s_waitcnt vmcnt(19) lgkmcnt(4)
	v_mfma_f32_16x16x32_f16 v[164:167], v[58:61], v[122:125], v[240:243]
	s_load_dword s30, s[12:13], 0x0
	v_cvt_pk_f16_f32 v142, v208, v209
	v_cvt_pk_f16_f32 v143, v210, v211
	v_mfma_f32_16x16x32_f16 v[168:171], v[58:61], v[126:129], v[240:243]
	v_pk_max_f16 v142, v142, 0
	v_pk_max_f16 v143, v143, 0
	v_mfma_f32_16x16x32_f16 v[172:175], v[58:61], v[134:137], v[240:243]
	v_cvt_pk_f16_f32 v144, v224, v225
	v_cvt_pk_f16_f32 v145, v226, v227
	v_mfma_f32_16x16x32_f16 v[10:13], v[58:61], v[138:141], v[240:243]
	v_pk_max_f16 v144, v144, 0
	v_pk_max_f16 v145, v145, 0
	ds_write_b128 v108, v[142:145]
	s_waitcnt vmcnt(18)
	v_mfma_f32_16x16x32_f16 v[58:61], v[54:57], v[122:125], v[244:247]
	v_cvt_pk_f16_f32 v152, v212, v213
	v_cvt_pk_f16_f32 v153, v214, v215
	v_mfma_f32_16x16x32_f16 v[176:179], v[54:57], v[126:129], v[244:247]
	v_pk_max_f16 v152, v152, 0
	v_pk_max_f16 v153, v153, 0
	v_mfma_f32_16x16x32_f16 v[180:183], v[54:57], v[134:137], v[244:247]
	v_cvt_pk_f16_f32 v154, v228, v229
	v_cvt_pk_f16_f32 v155, v230, v231
	v_mfma_f32_16x16x32_f16 v[18:21], v[54:57], v[138:141], v[244:247]
	v_pk_max_f16 v154, v154, 0
	v_pk_max_f16 v155, v155, 0
	ds_write_b128 v108, v[152:155] offset:16384
	s_waitcnt vmcnt(17)
	v_mfma_f32_16x16x32_f16 v[54:57], v[50:53], v[122:125], v[248:251]
	v_cvt_pk_f16_f32 v156, v216, v217
	v_cvt_pk_f16_f32 v157, v218, v219
	v_mfma_f32_16x16x32_f16 v[184:187], v[50:53], v[126:129], v[248:251]
	v_pk_max_f16 v156, v156, 0
	v_pk_max_f16 v157, v157, 0
	v_mfma_f32_16x16x32_f16 v[188:191], v[50:53], v[134:137], v[248:251]
	v_cvt_pk_f16_f32 v158, v232, v233
	v_cvt_pk_f16_f32 v159, v234, v235
	v_mfma_f32_16x16x32_f16 v[22:25], v[50:53], v[138:141], v[248:251]
	v_pk_max_f16 v158, v158, 0
	v_pk_max_f16 v159, v159, 0
	ds_write_b128 v108, v[156:159] offset:32768
	s_waitcnt vmcnt(16)
	v_mfma_f32_16x16x32_f16 v[50:53], v[38:41], v[122:125], v[252:255]
	v_cvt_pk_f16_f32 v160, v220, v221
	v_cvt_pk_f16_f32 v161, v222, v223
	v_mfma_f32_16x16x32_f16 v[122:125], v[38:41], v[126:129], v[252:255]
	v_pk_max_f16 v160, v160, 0
	v_pk_max_f16 v161, v161, 0
	v_mfma_f32_16x16x32_f16 v[126:129], v[38:41], v[134:137], v[252:255]
	v_cvt_pk_f16_f32 v162, v236, v237
	v_cvt_pk_f16_f32 v163, v238, v239
	v_mfma_f32_16x16x32_f16 v[38:41], v[38:41], v[138:141], v[252:255]
	v_pk_max_f16 v162, v162, 0
	v_pk_max_f16 v163, v163, 0
	ds_write_b128 v108, v[160:163] offset:49152
	s_add_i32 s9, s22, s35
	s_waitcnt vmcnt(15)
	v_mfma_f32_16x16x32_f16 v[164:167], v[94:97], v[142:145], v[164:167]
	v_mfma_f32_16x16x32_f16 v[168:171], v[94:97], v[152:155], v[168:171]
	s_waitcnt vmcnt(14)
	v_mfma_f32_16x16x32_f16 v[58:61], v[90:93], v[142:145], v[58:61]
	v_mfma_f32_16x16x32_f16 v[176:179], v[90:93], v[152:155], v[176:179]
	s_waitcnt vmcnt(13)
	v_mfma_f32_16x16x32_f16 v[54:57], v[78:81], v[142:145], v[54:57]
	v_mfma_f32_16x16x32_f16 v[184:187], v[78:81], v[152:155], v[184:187]
	s_waitcnt vmcnt(12)
	v_mfma_f32_16x16x32_f16 v[50:53], v[34:37], v[142:145], v[50:53]
	buffer_load_dwordx4 v[140:143], v147, s[16:19], s9 offen
	buffer_load_dwordx4 v[220:223], v148, s[16:19], s9 offen
	v_mfma_f32_16x16x32_f16 v[122:125], v[34:37], v[152:155], v[122:125]
	buffer_load_dwordx4 v[152:155], v149, s[16:19], s9 offen
	buffer_load_dwordx4 v[224:227], v150, s[16:19], s9 offen
	s_mov_b32 s9, s21
	s_waitcnt lgkmcnt(0)
	s_barrier
	v_add_u32_e32 v99, s66, v99
	ds_read_b128 v[136:139], v99
	ds_read_b128 v[208:211], v99 offset:16384
	ds_read_b128 v[212:215], v99 offset:32768
	ds_read_b128 v[216:219], v99 offset:49152
	v_mfma_f32_16x16x32_f16 v[172:175], v[94:97], v[156:159], v[172:175]
	v_mfma_f32_16x16x32_f16 v[94:97], v[94:97], v[160:163], v[10:13]
	s_nop 2
	v_lshl_add_u64 v[10:11], s[8:9], 4, v[130:131]
	v_mfma_f32_16x16x32_f16 v[180:183], v[90:93], v[156:159], v[180:183]
	v_mfma_f32_16x16x32_f16 v[90:93], v[90:93], v[160:163], v[18:21]
	v_mfma_f32_16x16x32_f16 v[188:191], v[78:81], v[156:159], v[188:191]
	v_mfma_f32_16x16x32_f16 v[78:81], v[78:81], v[160:163], v[22:25]
	global_load_dwordx4 v[30:33], v[10:11], off
	s_nop 1
	global_load_dwordx4 v[22:25], v[10:11], off offset:1024
	global_load_dwordx4 v[18:21], v[10:11], off offset:2048
	s_nop 0
	global_load_dwordx4 v[10:13], v[10:11], off offset:3072
	s_nop 0
	global_load_dwordx2 v[134:135], v[0:1], off
	v_mfma_f32_16x16x32_f16 v[126:129], v[34:37], v[156:159], v[126:129]
	v_mfma_f32_16x16x32_f16 v[34:37], v[34:37], v[160:163], v[38:41]
	s_nop 2
	v_add_u32_e32 v100, s67, v100
	ds_read_b128 v[38:41], v100
	ds_read_b128 v[156:159], v100 offset:16384
	ds_read_b128 v[160:163], v100 offset:32768
	ds_read_b128 v[228:231], v100 offset:49152
	s_add_i32 s8, s22, s36
	s_waitcnt vmcnt(20) lgkmcnt(7)
	v_mfma_f32_16x16x32_f16 v[164:167], v[82:85], v[136:139], v[164:167]
	s_waitcnt lgkmcnt(6)
	v_mfma_f32_16x16x32_f16 v[168:171], v[82:85], v[208:211], v[168:171]
	s_waitcnt lgkmcnt(5)
	v_mfma_f32_16x16x32_f16 v[172:175], v[82:85], v[212:215], v[172:175]
	s_waitcnt lgkmcnt(4)
	v_mfma_f32_16x16x32_f16 v[82:85], v[82:85], v[216:219], v[94:97]
	s_waitcnt vmcnt(19)
	v_mfma_f32_16x16x32_f16 v[58:61], v[70:73], v[136:139], v[58:61]
	v_mfma_f32_16x16x32_f16 v[94:97], v[70:73], v[208:211], v[176:179]
	v_mfma_f32_16x16x32_f16 v[176:179], v[70:73], v[212:215], v[180:183]
	v_mfma_f32_16x16x32_f16 v[70:73], v[70:73], v[216:219], v[90:93]
	s_waitcnt vmcnt(18)
	v_mfma_f32_16x16x32_f16 v[54:57], v[62:65], v[136:139], v[54:57]
	v_mfma_f32_16x16x32_f16 v[90:93], v[62:65], v[208:211], v[184:187]
	v_mfma_f32_16x16x32_f16 v[180:183], v[62:65], v[212:215], v[188:191]
	v_mfma_f32_16x16x32_f16 v[62:65], v[62:65], v[216:219], v[78:81]
	s_waitcnt vmcnt(17)
	v_mfma_f32_16x16x32_f16 v[50:53], v[42:45], v[136:139], v[50:53]
	v_mfma_f32_16x16x32_f16 v[78:81], v[42:45], v[208:211], v[122:125]
	v_mfma_f32_16x16x32_f16 v[122:125], v[42:45], v[212:215], v[126:129]
	s_nop 2
	buffer_load_dwordx4 v[126:129], v147, s[16:19], s8 offen
	buffer_load_dwordx4 v[136:139], v148, s[16:19], s8 offen
	buffer_load_dwordx4 v[184:187], v149, s[16:19], s8 offen
	buffer_load_dwordx4 v[188:191], v150, s[16:19], s8 offen
	v_mfma_f32_16x16x32_f16 v[34:37], v[42:45], v[216:219], v[34:37]
	v_add_u32_e32 v111, s68, v111
	ds_read_b128 v[42:45], v111
	ds_read_b128 v[208:211], v111 offset:16384
	ds_read_b128 v[212:215], v111 offset:32768
	ds_read_b128 v[216:219], v111 offset:49152
	s_add_i32 s8, s22, s37
	s_waitcnt vmcnt(20) lgkmcnt(7)
	v_mfma_f32_16x16x32_f16 v[164:167], v[86:89], v[38:41], v[164:167]
	s_waitcnt lgkmcnt(6)
	v_mfma_f32_16x16x32_f16 v[168:171], v[86:89], v[156:159], v[168:171]
	s_waitcnt lgkmcnt(5)
	v_mfma_f32_16x16x32_f16 v[172:175], v[86:89], v[160:163], v[172:175]
	s_waitcnt lgkmcnt(4)
	v_mfma_f32_16x16x32_f16 v[82:85], v[86:89], v[228:231], v[82:85]
	s_waitcnt vmcnt(19)
	v_mfma_f32_16x16x32_f16 v[58:61], v[74:77], v[38:41], v[58:61]
	v_mfma_f32_16x16x32_f16 v[86:89], v[74:77], v[156:159], v[94:97]
	v_mfma_f32_16x16x32_f16 v[94:97], v[74:77], v[160:163], v[176:179]
	v_mfma_f32_16x16x32_f16 v[70:73], v[74:77], v[228:231], v[70:73]
	s_waitcnt vmcnt(18)
	v_mfma_f32_16x16x32_f16 v[54:57], v[66:69], v[38:41], v[54:57]
	v_mfma_f32_16x16x32_f16 v[74:77], v[66:69], v[156:159], v[90:93]
	v_mfma_f32_16x16x32_f16 v[90:93], v[66:69], v[160:163], v[180:183]
	v_mfma_f32_16x16x32_f16 v[62:65], v[66:69], v[228:231], v[62:65]
	s_waitcnt vmcnt(17)
	v_mfma_f32_16x16x32_f16 v[38:41], v[46:49], v[38:41], v[50:53]
	v_mfma_f32_16x16x32_f16 v[50:53], v[46:49], v[156:159], v[78:81]
	v_mfma_f32_16x16x32_f16 v[66:69], v[46:49], v[160:163], v[122:125]
	s_nop 1
	buffer_load_dwordx4 v[78:81], v147, s[16:19], s8 offen
	buffer_load_dwordx4 v[122:125], v148, s[16:19], s8 offen
	buffer_load_dwordx4 v[156:159], v149, s[16:19], s8 offen
	buffer_load_dwordx4 v[160:163], v150, s[16:19], s8 offen
	v_mfma_f32_16x16x32_f16 v[34:37], v[46:49], v[228:231], v[34:37]
	v_add_u32_e32 v98, s69, v98
	ds_read_b128 v[46:49], v98
	ds_read_b128 v[176:179], v98 offset:16384
	ds_read_b128 v[180:183], v98 offset:32768
	ds_read_b128 v[228:231], v98 offset:49152
	s_add_i32 s8, s22, s38
	s_waitcnt vmcnt(20) lgkmcnt(7)
	v_mfma_f32_16x16x32_f16 v[164:167], v[192:195], v[42:45], v[164:167]
	s_waitcnt lgkmcnt(6)
	v_mfma_f32_16x16x32_f16 v[168:171], v[192:195], v[208:211], v[168:171]
	s_waitcnt lgkmcnt(5)
	v_mfma_f32_16x16x32_f16 v[172:175], v[192:195], v[212:215], v[172:175]
	s_waitcnt lgkmcnt(4)
	v_mfma_f32_16x16x32_f16 v[82:85], v[192:195], v[216:219], v[82:85]
	s_waitcnt vmcnt(19)
	v_mfma_f32_16x16x32_f16 v[58:61], v[196:199], v[42:45], v[58:61]
	v_mfma_f32_16x16x32_f16 v[86:89], v[196:199], v[208:211], v[86:89]
	v_mfma_f32_16x16x32_f16 v[94:97], v[196:199], v[212:215], v[94:97]
	v_mfma_f32_16x16x32_f16 v[70:73], v[196:199], v[216:219], v[70:73]
	s_waitcnt vmcnt(18)
	v_mfma_f32_16x16x32_f16 v[54:57], v[200:203], v[42:45], v[54:57]
	v_mfma_f32_16x16x32_f16 v[74:77], v[200:203], v[208:211], v[74:77]
	v_mfma_f32_16x16x32_f16 v[90:93], v[200:203], v[212:215], v[90:93]
	v_mfma_f32_16x16x32_f16 v[62:65], v[200:203], v[216:219], v[62:65]
	s_waitcnt vmcnt(17)
	v_mfma_f32_16x16x32_f16 v[38:41], v[204:207], v[42:45], v[38:41]
	v_mfma_f32_16x16x32_f16 v[42:45], v[204:207], v[208:211], v[50:53]
	v_mfma_f32_16x16x32_f16 v[50:53], v[204:207], v[212:215], v[66:69]
	s_nop 2
	buffer_load_dwordx4 v[66:69], v147, s[16:19], s8 offen
	buffer_load_dwordx4 v[192:195], v148, s[16:19], s8 offen
	buffer_load_dwordx4 v[196:199], v149, s[16:19], s8 offen
	buffer_load_dwordx4 v[200:203], v150, s[16:19], s8 offen
	v_mfma_f32_16x16x32_f16 v[34:37], v[204:207], v[216:219], v[34:37]
	v_add_u32_e32 v99, s70, v99
	ds_read_b128 v[204:207], v99
	ds_read_b128 v[208:211], v99 offset:16384
	ds_read_b128 v[212:215], v99 offset:32768
	ds_read_b128 v[216:219], v99 offset:49152
	s_add_i32 s8, s22, s39
	s_waitcnt vmcnt(20) lgkmcnt(7)
	v_mfma_f32_16x16x32_f16 v[164:167], v[140:143], v[46:49], v[164:167]
	s_waitcnt lgkmcnt(6)
	v_mfma_f32_16x16x32_f16 v[168:171], v[140:143], v[176:179], v[168:171]
	s_waitcnt lgkmcnt(5)
	v_mfma_f32_16x16x32_f16 v[172:175], v[140:143], v[180:183], v[172:175]
	s_waitcnt lgkmcnt(4)
	v_mfma_f32_16x16x32_f16 v[82:85], v[140:143], v[228:231], v[82:85]
	s_waitcnt vmcnt(19)
	v_mfma_f32_16x16x32_f16 v[58:61], v[220:223], v[46:49], v[58:61]
	v_mfma_f32_16x16x32_f16 v[86:89], v[220:223], v[176:179], v[86:89]
	s_waitcnt vmcnt(18)
	v_mfma_f32_16x16x32_f16 v[54:57], v[152:155], v[46:49], v[54:57]
	v_mfma_f32_16x16x32_f16 v[74:77], v[152:155], v[176:179], v[74:77]
	v_mfma_f32_16x16x32_f16 v[90:93], v[152:155], v[180:183], v[90:93]
	v_mfma_f32_16x16x32_f16 v[62:65], v[152:155], v[228:231], v[62:65]
	s_waitcnt vmcnt(17)
	v_mfma_f32_16x16x32_f16 v[38:41], v[224:227], v[46:49], v[38:41]
	v_mfma_f32_16x16x32_f16 v[42:45], v[224:227], v[176:179], v[42:45]
	v_mfma_f32_16x16x32_f16 v[46:49], v[224:227], v[180:183], v[50:53]
	s_nop 2
	buffer_load_dwordx4 v[50:53], v147, s[16:19], s8 offen
	buffer_load_dwordx4 v[140:143], v148, s[16:19], s8 offen
	buffer_load_dwordx4 v[152:155], v149, s[16:19], s8 offen
	buffer_load_dwordx4 v[176:179], v150, s[16:19], s8 offen
	v_mfma_f32_16x16x32_f16 v[94:97], v[220:223], v[180:183], v[94:97]
	v_mfma_f32_16x16x32_f16 v[70:73], v[220:223], v[228:231], v[70:73]
	v_mfma_f32_16x16x32_f16 v[34:37], v[224:227], v[228:231], v[34:37]
	v_add_u32_e32 v100, s71, v100
	ds_read_b128 v[180:183], v100
	ds_read_b128 v[220:223], v100 offset:16384
	ds_read_b128 v[224:227], v100 offset:32768
	ds_read_b128 v[228:231], v100 offset:49152
	s_add_i32 s8, s22, s40
	s_waitcnt vmcnt(15) lgkmcnt(7)
	v_mfma_f32_16x16x32_f16 v[164:167], v[126:129], v[204:207], v[164:167]
	s_waitcnt lgkmcnt(6)
	v_mfma_f32_16x16x32_f16 v[168:171], v[126:129], v[208:211], v[168:171]
	s_waitcnt lgkmcnt(5)
	v_mfma_f32_16x16x32_f16 v[172:175], v[126:129], v[212:215], v[172:175]
	s_waitcnt lgkmcnt(4)
	v_mfma_f32_16x16x32_f16 v[82:85], v[126:129], v[216:219], v[82:85]
	s_waitcnt vmcnt(14)
	v_mfma_f32_16x16x32_f16 v[58:61], v[136:139], v[204:207], v[58:61]
	v_mfma_f32_16x16x32_f16 v[86:89], v[136:139], v[208:211], v[86:89]
	v_mfma_f32_16x16x32_f16 v[94:97], v[136:139], v[212:215], v[94:97]
	v_mfma_f32_16x16x32_f16 v[70:73], v[136:139], v[216:219], v[70:73]
	s_waitcnt vmcnt(13)
	v_mfma_f32_16x16x32_f16 v[54:57], v[184:187], v[204:207], v[54:57]
	v_mfma_f32_16x16x32_f16 v[74:77], v[184:187], v[208:211], v[74:77]
	v_mfma_f32_16x16x32_f16 v[90:93], v[184:187], v[212:215], v[90:93]
	v_mfma_f32_16x16x32_f16 v[62:65], v[184:187], v[216:219], v[62:65]
	s_waitcnt vmcnt(12)
	v_mfma_f32_16x16x32_f16 v[38:41], v[188:191], v[204:207], v[38:41]
	buffer_load_dwordx4 v[126:129], v147, s[16:19], s8 offen
	buffer_load_dwordx4 v[136:139], v148, s[16:19], s8 offen
	buffer_load_dwordx4 v[184:187], v149, s[16:19], s8 offen
	buffer_load_dwordx4 v[204:207], v150, s[16:19], s8 offen
	v_mfma_f32_16x16x32_f16 v[42:45], v[188:191], v[208:211], v[42:45]
	v_mfma_f32_16x16x32_f16 v[46:49], v[188:191], v[212:215], v[46:49]
	v_mfma_f32_16x16x32_f16 v[34:37], v[188:191], v[216:219], v[34:37]
	v_add_u32_e32 v111, s72, v111
	ds_read_b128 v[188:191], v111
	ds_read_b128 v[208:211], v111 offset:16384
	ds_read_b128 v[212:215], v111 offset:32768
	ds_read_b128 v[216:219], v111 offset:49152
	s_add_i32 s8, s22, s41
	s_waitcnt vmcnt(15) lgkmcnt(7)
	v_mfma_f32_16x16x32_f16 v[164:167], v[78:81], v[180:183], v[164:167]
	s_waitcnt lgkmcnt(6)
	v_mfma_f32_16x16x32_f16 v[168:171], v[78:81], v[220:223], v[168:171]
	s_waitcnt lgkmcnt(5)
	v_mfma_f32_16x16x32_f16 v[172:175], v[78:81], v[224:227], v[172:175]
	s_waitcnt lgkmcnt(4)
	v_mfma_f32_16x16x32_f16 v[78:81], v[78:81], v[228:231], v[82:85]
	s_waitcnt vmcnt(14)
	v_mfma_f32_16x16x32_f16 v[58:61], v[122:125], v[180:183], v[58:61]
	v_mfma_f32_16x16x32_f16 v[82:85], v[122:125], v[220:223], v[86:89]
	v_mfma_f32_16x16x32_f16 v[86:89], v[122:125], v[224:227], v[94:97]
	v_mfma_f32_16x16x32_f16 v[70:73], v[122:125], v[228:231], v[70:73]
	s_waitcnt vmcnt(13)
	v_mfma_f32_16x16x32_f16 v[54:57], v[156:159], v[180:183], v[54:57]
	v_mfma_f32_16x16x32_f16 v[74:77], v[156:159], v[220:223], v[74:77]
	v_mfma_f32_16x16x32_f16 v[90:93], v[156:159], v[224:227], v[90:93]
	v_mfma_f32_16x16x32_f16 v[62:65], v[156:159], v[228:231], v[62:65]
	s_waitcnt vmcnt(12)
	v_mfma_f32_16x16x32_f16 v[38:41], v[160:163], v[180:183], v[38:41]
	buffer_load_dwordx4 v[94:97], v147, s[16:19], s8 offen
	buffer_load_dwordx4 v[122:125], v148, s[16:19], s8 offen
	buffer_load_dwordx4 v[156:159], v149, s[16:19], s8 offen
	buffer_load_dwordx4 v[180:183], v150, s[16:19], s8 offen
	v_mfma_f32_16x16x32_f16 v[42:45], v[160:163], v[220:223], v[42:45]
	v_mfma_f32_16x16x32_f16 v[46:49], v[160:163], v[224:227], v[46:49]
	v_mfma_f32_16x16x32_f16 v[34:37], v[160:163], v[228:231], v[34:37]
	v_add_u32_e32 v98, s73, v98
	ds_read_b128 v[160:163], v98
	ds_read_b128 v[220:223], v98 offset:16384
	ds_read_b128 v[224:227], v98 offset:32768
	ds_read_b128 v[228:231], v98 offset:49152
	s_add_i32 s8, s22, s42
	s_waitcnt vmcnt(15) lgkmcnt(7)
	v_mfma_f32_16x16x32_f16 v[164:167], v[66:69], v[188:191], v[164:167]
	s_waitcnt lgkmcnt(6)
	v_mfma_f32_16x16x32_f16 v[168:171], v[66:69], v[208:211], v[168:171]
	s_waitcnt lgkmcnt(5)
	v_mfma_f32_16x16x32_f16 v[172:175], v[66:69], v[212:215], v[172:175]
	s_waitcnt lgkmcnt(4)
	v_mfma_f32_16x16x32_f16 v[66:69], v[66:69], v[216:219], v[78:81]
	s_waitcnt vmcnt(14)
	v_mfma_f32_16x16x32_f16 v[58:61], v[192:195], v[188:191], v[58:61]
	v_mfma_f32_16x16x32_f16 v[78:81], v[192:195], v[208:211], v[82:85]
	v_mfma_f32_16x16x32_f16 v[82:85], v[192:195], v[212:215], v[86:89]
	v_mfma_f32_16x16x32_f16 v[70:73], v[192:195], v[216:219], v[70:73]
	s_waitcnt vmcnt(13)
	v_mfma_f32_16x16x32_f16 v[54:57], v[196:199], v[188:191], v[54:57]
	v_mfma_f32_16x16x32_f16 v[74:77], v[196:199], v[208:211], v[74:77]
	v_mfma_f32_16x16x32_f16 v[86:89], v[196:199], v[212:215], v[90:93]
	v_mfma_f32_16x16x32_f16 v[62:65], v[196:199], v[216:219], v[62:65]
	s_waitcnt vmcnt(12)
	v_mfma_f32_16x16x32_f16 v[38:41], v[200:203], v[188:191], v[38:41]
	buffer_load_dwordx4 v[90:93], v147, s[16:19], s8 offen
	buffer_load_dwordx4 v[188:191], v148, s[16:19], s8 offen
	buffer_load_dwordx4 v[192:195], v149, s[16:19], s8 offen
	buffer_load_dwordx4 v[196:199], v150, s[16:19], s8 offen
	v_mfma_f32_16x16x32_f16 v[42:45], v[200:203], v[208:211], v[42:45]
	v_mfma_f32_16x16x32_f16 v[46:49], v[200:203], v[212:215], v[46:49]
	v_mfma_f32_16x16x32_f16 v[34:37], v[200:203], v[216:219], v[34:37]
	v_add_u32_e32 v99, s74, v99
	ds_read_b128 v[200:203], v99
	ds_read_b128 v[208:211], v99 offset:16384
	ds_read_b128 v[212:215], v99 offset:32768
	ds_read_b128 v[216:219], v99 offset:49152
	s_add_i32 s8, s22, s43
	s_waitcnt vmcnt(15) lgkmcnt(7)
	v_mfma_f32_16x16x32_f16 v[164:167], v[50:53], v[160:163], v[164:167]
	s_waitcnt lgkmcnt(6)
	v_mfma_f32_16x16x32_f16 v[168:171], v[50:53], v[220:223], v[168:171]
	s_waitcnt lgkmcnt(5)
	v_mfma_f32_16x16x32_f16 v[172:175], v[50:53], v[224:227], v[172:175]
	s_waitcnt lgkmcnt(4)
	v_mfma_f32_16x16x32_f16 v[50:53], v[50:53], v[228:231], v[66:69]
	s_waitcnt vmcnt(14)
	v_mfma_f32_16x16x32_f16 v[58:61], v[140:143], v[160:163], v[58:61]
	v_mfma_f32_16x16x32_f16 v[66:69], v[140:143], v[220:223], v[78:81]
	v_mfma_f32_16x16x32_f16 v[78:81], v[140:143], v[224:227], v[82:85]
	v_mfma_f32_16x16x32_f16 v[70:73], v[140:143], v[228:231], v[70:73]
	s_waitcnt vmcnt(13)
	v_mfma_f32_16x16x32_f16 v[54:57], v[152:155], v[160:163], v[54:57]
	v_mfma_f32_16x16x32_f16 v[74:77], v[152:155], v[220:223], v[74:77]
	v_mfma_f32_16x16x32_f16 v[82:85], v[152:155], v[224:227], v[86:89]
	v_mfma_f32_16x16x32_f16 v[62:65], v[152:155], v[228:231], v[62:65]
	s_waitcnt vmcnt(12)
	v_mfma_f32_16x16x32_f16 v[38:41], v[176:179], v[160:163], v[38:41]
	buffer_load_dwordx4 v[86:89], v147, s[16:19], s8 offen
	buffer_load_dwordx4 v[140:143], v148, s[16:19], s8 offen
	buffer_load_dwordx4 v[152:155], v149, s[16:19], s8 offen
	buffer_load_dwordx4 v[160:163], v150, s[16:19], s8 offen
	v_mfma_f32_16x16x32_f16 v[42:45], v[176:179], v[220:223], v[42:45]
	v_mfma_f32_16x16x32_f16 v[46:49], v[176:179], v[224:227], v[46:49]
	v_mfma_f32_16x16x32_f16 v[34:37], v[176:179], v[228:231], v[34:37]
	v_add_u32_e32 v100, s75, v100
	ds_read_b128 v[176:179], v100
	ds_read_b128 v[220:223], v100 offset:16384
	ds_read_b128 v[224:227], v100 offset:32768
	ds_read_b128 v[228:231], v100 offset:49152
	s_add_i32 s8, s22, s44
	s_waitcnt vmcnt(15) lgkmcnt(7)
	v_mfma_f32_16x16x32_f16 v[164:167], v[126:129], v[200:203], v[164:167]
	s_waitcnt lgkmcnt(6)
	v_mfma_f32_16x16x32_f16 v[168:171], v[126:129], v[208:211], v[168:171]
	s_waitcnt lgkmcnt(5)
	v_mfma_f32_16x16x32_f16 v[172:175], v[126:129], v[212:215], v[172:175]
	s_waitcnt lgkmcnt(4)
	v_mfma_f32_16x16x32_f16 v[50:53], v[126:129], v[216:219], v[50:53]
	s_waitcnt vmcnt(14)
	v_mfma_f32_16x16x32_f16 v[58:61], v[136:139], v[200:203], v[58:61]
	v_mfma_f32_16x16x32_f16 v[66:69], v[136:139], v[208:211], v[66:69]
	v_mfma_f32_16x16x32_f16 v[78:81], v[136:139], v[212:215], v[78:81]
	v_mfma_f32_16x16x32_f16 v[70:73], v[136:139], v[216:219], v[70:73]
	s_waitcnt vmcnt(13)
	v_mfma_f32_16x16x32_f16 v[54:57], v[184:187], v[200:203], v[54:57]
	v_mfma_f32_16x16x32_f16 v[74:77], v[184:187], v[208:211], v[74:77]
	v_mfma_f32_16x16x32_f16 v[82:85], v[184:187], v[212:215], v[82:85]
	v_mfma_f32_16x16x32_f16 v[62:65], v[184:187], v[216:219], v[62:65]
	s_waitcnt vmcnt(12)
	v_mfma_f32_16x16x32_f16 v[38:41], v[204:207], v[200:203], v[38:41]
	buffer_load_dwordx4 v[126:129], v147, s[16:19], s8 offen
	buffer_load_dwordx4 v[136:139], v148, s[16:19], s8 offen
	buffer_load_dwordx4 v[184:187], v149, s[16:19], s8 offen
	buffer_load_dwordx4 v[200:203], v150, s[16:19], s8 offen
	v_mfma_f32_16x16x32_f16 v[42:45], v[204:207], v[208:211], v[42:45]
	v_mfma_f32_16x16x32_f16 v[46:49], v[204:207], v[212:215], v[46:49]
	v_mfma_f32_16x16x32_f16 v[34:37], v[204:207], v[216:219], v[34:37]
	v_add_u32_e32 v111, s76, v111
	ds_read_b128 v[204:207], v111
	ds_read_b128 v[208:211], v111 offset:16384
	ds_read_b128 v[212:215], v111 offset:32768
	ds_read_b128 v[216:219], v111 offset:49152
	s_add_i32 s8, s22, s45
	s_waitcnt vmcnt(15) lgkmcnt(7)
	v_mfma_f32_16x16x32_f16 v[164:167], v[94:97], v[176:179], v[164:167]
	s_waitcnt lgkmcnt(6)
	v_mfma_f32_16x16x32_f16 v[168:171], v[94:97], v[220:223], v[168:171]
	s_waitcnt vmcnt(14)
	v_mfma_f32_16x16x32_f16 v[58:61], v[122:125], v[176:179], v[58:61]
	v_mfma_f32_16x16x32_f16 v[66:69], v[122:125], v[220:223], v[66:69]
	s_waitcnt lgkmcnt(5)
	v_mfma_f32_16x16x32_f16 v[78:81], v[122:125], v[224:227], v[78:81]
	s_waitcnt lgkmcnt(4)
	v_mfma_f32_16x16x32_f16 v[70:73], v[122:125], v[228:231], v[70:73]
	s_waitcnt vmcnt(13)
	v_mfma_f32_16x16x32_f16 v[54:57], v[156:159], v[176:179], v[54:57]
	v_mfma_f32_16x16x32_f16 v[74:77], v[156:159], v[220:223], v[74:77]
	v_mfma_f32_16x16x32_f16 v[82:85], v[156:159], v[224:227], v[82:85]
	v_mfma_f32_16x16x32_f16 v[62:65], v[156:159], v[228:231], v[62:65]
	s_waitcnt vmcnt(12)
	v_mfma_f32_16x16x32_f16 v[38:41], v[180:183], v[176:179], v[38:41]
	v_mfma_f32_16x16x32_f16 v[42:45], v[180:183], v[220:223], v[42:45]
	buffer_load_dwordx4 v[122:125], v147, s[16:19], s8 offen
	buffer_load_dwordx4 v[156:159], v148, s[16:19], s8 offen
	buffer_load_dwordx4 v[176:179], v149, s[16:19], s8 offen
	buffer_load_dwordx4 v[220:223], v150, s[16:19], s8 offen
	v_mfma_f32_16x16x32_f16 v[50:53], v[94:97], v[228:231], v[50:53]
	v_mfma_f32_16x16x32_f16 v[46:49], v[180:183], v[224:227], v[46:49]
	v_mfma_f32_16x16x32_f16 v[34:37], v[180:183], v[228:231], v[34:37]
	v_mfma_f32_16x16x32_f16 v[172:175], v[94:97], v[224:227], v[172:175]
	v_add_u32_e32 v98, s77, v98
	ds_read_b128 v[94:97], v98
	ds_read_b128 v[180:183], v98 offset:16384
	ds_read_b128 v[224:227], v98 offset:32768
	ds_read_b128 v[228:231], v98 offset:49152
	s_add_i32 s8, s22, s46
	s_waitcnt vmcnt(15) lgkmcnt(7)
	v_mfma_f32_16x16x32_f16 v[164:167], v[90:93], v[204:207], v[164:167]
	s_waitcnt lgkmcnt(6)
	v_mfma_f32_16x16x32_f16 v[168:171], v[90:93], v[208:211], v[168:171]
	s_waitcnt lgkmcnt(5)
	v_mfma_f32_16x16x32_f16 v[172:175], v[90:93], v[212:215], v[172:175]
	s_waitcnt lgkmcnt(4)
	v_mfma_f32_16x16x32_f16 v[90:93], v[90:93], v[216:219], v[50:53]
	s_waitcnt vmcnt(14)
	v_mfma_f32_16x16x32_f16 v[232:235], v[188:191], v[204:207], v[58:61]
	v_mfma_f32_16x16x32_f16 v[66:69], v[188:191], v[208:211], v[66:69]
	v_mfma_f32_16x16x32_f16 v[78:81], v[188:191], v[212:215], v[78:81]
	v_mfma_f32_16x16x32_f16 v[70:73], v[188:191], v[216:219], v[70:73]
	s_waitcnt vmcnt(13)
	v_mfma_f32_16x16x32_f16 v[188:191], v[192:195], v[204:207], v[54:57]
	v_mfma_f32_16x16x32_f16 v[74:77], v[192:195], v[208:211], v[74:77]
	v_mfma_f32_16x16x32_f16 v[82:85], v[192:195], v[212:215], v[82:85]
	v_mfma_f32_16x16x32_f16 v[62:65], v[192:195], v[216:219], v[62:65]
	s_waitcnt vmcnt(12)
	v_mfma_f32_16x16x32_f16 v[192:195], v[196:199], v[204:207], v[38:41]
	buffer_load_dwordx4 v[58:61], v147, s[16:19], s8 offen
	buffer_load_dwordx4 v[54:57], v148, s[16:19], s8 offen
	buffer_load_dwordx4 v[50:53], v149, s[16:19], s8 offen
	buffer_load_dwordx4 v[38:41], v150, s[16:19], s8 offen
	v_mfma_f32_16x16x32_f16 v[42:45], v[196:199], v[208:211], v[42:45]
	v_mfma_f32_16x16x32_f16 v[46:49], v[196:199], v[212:215], v[46:49]
	v_mfma_f32_16x16x32_f16 v[196:199], v[196:199], v[216:219], v[34:37]
	v_add_u32_e32 v99, s78, v99
	ds_read_b128 v[204:207], v99
	ds_read_b128 v[208:211], v99 offset:16384
	ds_read_b128 v[212:215], v99 offset:32768
	ds_read_b128 v[216:219], v99 offset:49152
	s_add_i32 s8, s22, s47
	s_waitcnt vmcnt(15) lgkmcnt(7)
	v_mfma_f32_16x16x32_f16 v[164:167], v[86:89], v[94:97], v[164:167]
	s_waitcnt lgkmcnt(6)
	v_mfma_f32_16x16x32_f16 v[168:171], v[86:89], v[180:183], v[168:171]
	s_waitcnt lgkmcnt(5)
	v_mfma_f32_16x16x32_f16 v[172:175], v[86:89], v[224:227], v[172:175]
	s_waitcnt lgkmcnt(4)
	v_mfma_f32_16x16x32_f16 v[86:89], v[86:89], v[228:231], v[90:93]
	s_waitcnt vmcnt(14)
	v_mfma_f32_16x16x32_f16 v[232:235], v[140:143], v[94:97], v[232:235]
	v_mfma_f32_16x16x32_f16 v[66:69], v[140:143], v[180:183], v[66:69]
	v_mfma_f32_16x16x32_f16 v[236:239], v[140:143], v[224:227], v[78:81]
	v_mfma_f32_16x16x32_f16 v[70:73], v[140:143], v[228:231], v[70:73]
	s_waitcnt vmcnt(13)
	v_mfma_f32_16x16x32_f16 v[140:143], v[152:155], v[94:97], v[188:191]
	v_mfma_f32_16x16x32_f16 v[74:77], v[152:155], v[180:183], v[74:77]
	v_mfma_f32_16x16x32_f16 v[82:85], v[152:155], v[224:227], v[82:85]
	v_mfma_f32_16x16x32_f16 v[62:65], v[152:155], v[228:231], v[62:65]
	s_waitcnt vmcnt(12)
	v_mfma_f32_16x16x32_f16 v[152:155], v[160:163], v[94:97], v[192:195]
	buffer_load_dwordx4 v[94:97], v147, s[16:19], s8 offen
	buffer_load_dwordx4 v[90:93], v148, s[16:19], s8 offen
	buffer_load_dwordx4 v[78:81], v149, s[16:19], s8 offen
	buffer_load_dwordx4 v[34:37], v150, s[16:19], s8 offen
	v_mfma_f32_16x16x32_f16 v[42:45], v[160:163], v[180:183], v[42:45]
	v_mfma_f32_16x16x32_f16 v[46:49], v[160:163], v[224:227], v[46:49]
	v_mfma_f32_16x16x32_f16 v[160:163], v[160:163], v[228:231], v[196:199]
	v_add_u32_e32 v100, s79, v100
	ds_read_b128 v[180:183], v100
	ds_read_b128 v[188:191], v100 offset:16384
	ds_read_b128 v[192:195], v100 offset:32768
	ds_read_b128 v[196:199], v100 offset:49152
	s_add_i32 s8, s22, s48
	s_waitcnt vmcnt(15) lgkmcnt(7)
	v_mfma_f32_16x16x32_f16 v[164:167], v[126:129], v[204:207], v[164:167]
	s_waitcnt lgkmcnt(6)
	v_mfma_f32_16x16x32_f16 v[168:171], v[126:129], v[208:211], v[168:171]
	s_waitcnt lgkmcnt(5)
	v_mfma_f32_16x16x32_f16 v[172:175], v[126:129], v[212:215], v[172:175]
	s_waitcnt lgkmcnt(4)
	v_mfma_f32_16x16x32_f16 v[86:89], v[126:129], v[216:219], v[86:89]
	s_waitcnt vmcnt(14)
	v_mfma_f32_16x16x32_f16 v[126:129], v[136:139], v[204:207], v[232:235]
	v_mfma_f32_16x16x32_f16 v[66:69], v[136:139], v[208:211], v[66:69]
	v_mfma_f32_16x16x32_f16 v[224:227], v[136:139], v[212:215], v[236:239]
	v_mfma_f32_16x16x32_f16 v[136:139], v[136:139], v[216:219], v[70:73]
	s_waitcnt vmcnt(13)
	v_mfma_f32_16x16x32_f16 v[140:143], v[184:187], v[204:207], v[140:143]
	v_mfma_f32_16x16x32_f16 v[74:77], v[184:187], v[208:211], v[74:77]
	v_mfma_f32_16x16x32_f16 v[228:231], v[184:187], v[212:215], v[82:85]
	v_mfma_f32_16x16x32_f16 v[184:187], v[184:187], v[216:219], v[62:65]
	s_waitcnt vmcnt(12)
	v_mfma_f32_16x16x32_f16 v[152:155], v[200:203], v[204:207], v[152:155]
	v_mfma_f32_16x16x32_f16 v[204:207], v[200:203], v[208:211], v[42:45]
	buffer_load_dwordx4 v[82:85], v147, s[16:19], s8 offen
	buffer_load_dwordx4 v[70:73], v148, s[16:19], s8 offen
	buffer_load_dwordx4 v[62:65], v149, s[16:19], s8 offen
	buffer_load_dwordx4 v[42:45], v150, s[16:19], s8 offen
	v_mfma_f32_16x16x32_f16 v[46:49], v[200:203], v[212:215], v[46:49]
	v_mfma_f32_16x16x32_f16 v[160:163], v[200:203], v[216:219], v[160:163]
	v_add_u32_e32 v0, 0x1ac00, v104
	ds_read_b128 v[240:243], v0
	ds_read_b128 v[244:247], v0 offset:16
	s_waitcnt vmcnt(12) lgkmcnt(5)
	v_mfma_f32_16x16x32_f16 v[164:167], v[122:125], v[180:183], v[164:167]
	v_mfma_f32_16x16x32_f16 v[126:129], v[156:159], v[180:183], v[126:129]
	v_mfma_f32_16x16x32_f16 v[140:143], v[176:179], v[180:183], v[140:143]
	v_mfma_f32_16x16x32_f16 v[152:155], v[220:223], v[180:183], v[152:155]
	s_waitcnt lgkmcnt(4)
	v_mfma_f32_16x16x32_f16 v[168:171], v[122:125], v[188:191], v[168:171]
	v_mfma_f32_16x16x32_f16 v[208:211], v[156:159], v[188:191], v[66:69]
	v_mfma_f32_16x16x32_f16 v[212:215], v[176:179], v[188:191], v[74:77]
	v_mfma_f32_16x16x32_f16 v[204:207], v[220:223], v[188:191], v[204:207]
	s_waitcnt lgkmcnt(3)
	v_mfma_f32_16x16x32_f16 v[172:175], v[122:125], v[192:195], v[172:175]
	v_cvt_pk_f16_f32 v232, v164, v165
	v_cvt_pk_f16_f32 v233, v166, v167
	v_pk_max_f16 v232, v232, 0
	v_pk_max_f16 v233, v233, 0
	v_mfma_f32_16x16x32_f16 v[224:227], v[156:159], v[192:195], v[224:227]
	v_cvt_pk_f16_f32 v234, v126, v127
	v_cvt_pk_f16_f32 v235, v128, v129
	v_pk_max_f16 v234, v234, 0
	v_pk_max_f16 v235, v235, 0
	v_mfma_f32_16x16x32_f16 v[228:231], v[176:179], v[192:195], v[228:231]
	v_cvt_pk_f16_f32 v236, v140, v141
	v_cvt_pk_f16_f32 v237, v142, v143
	v_pk_max_f16 v236, v236, 0
	v_pk_max_f16 v237, v237, 0
	v_mfma_f32_16x16x32_f16 v[216:219], v[220:223], v[192:195], v[46:49]
	v_cvt_pk_f16_f32 v238, v152, v153
	v_cvt_pk_f16_f32 v239, v154, v155
	v_pk_max_f16 v238, v238, 0
	v_pk_max_f16 v239, v239, 0
	s_waitcnt lgkmcnt(2)
	v_mfma_f32_16x16x32_f16 v[200:203], v[122:125], v[196:199], v[86:89]
	v_cvt_pk_f16_f32 v180, v168, v169
	v_cvt_pk_f16_f32 v181, v170, v171
	v_pk_max_f16 v180, v180, 0
	v_pk_max_f16 v181, v181, 0
	s_add_i32 s8, s22, s49
	buffer_load_dwordx4 v[86:89], v147, s[16:19], s8 offen
	buffer_load_dwordx4 v[74:77], v148, s[16:19], s8 offen
	buffer_load_dwordx4 v[66:69], v149, s[16:19], s8 offen
	buffer_load_dwordx4 v[46:49], v150, s[16:19], s8 offen
	v_mfma_f32_16x16x32_f16 v[136:139], v[156:159], v[196:199], v[136:139]
	v_cvt_pk_f16_f32 v182, v208, v209
	v_cvt_pk_f16_f32 v183, v210, v211
	v_pk_max_f16 v182, v182, 0
	v_pk_max_f16 v183, v183, 0
	s_waitcnt lgkmcnt(1)
	v_mfma_f32_16x16x32_f16 v[252:255], v[240:243], v[232:235], 0
	v_cvt_pk_f16_f32 v232, v172, v173
	v_cvt_pk_f16_f32 v233, v174, v175
	v_pk_max_f16 v232, v232, 0
	v_pk_max_f16 v233, v233, 0
	v_mfma_f32_16x16x32_f16 v[184:187], v[176:179], v[196:199], v[184:187]
	v_cvt_pk_f16_f32 v188, v212, v213
	v_cvt_pk_f16_f32 v189, v214, v215
	v_pk_max_f16 v188, v188, 0
	v_pk_max_f16 v189, v189, 0
	s_waitcnt lgkmcnt(0)
	v_mfma_f32_16x16x32_f16 v[252:255], v[244:247], v[236:239], v[252:255]
	ds_read_u16 v102, v114
	ds_read_u16 v103, v114 offset:512
	ds_read_u16 v115, v114 offset:1024
	ds_read_u16 v116, v114 offset:1536
	v_cvt_pk_f16_f32 v234, v224, v225
	v_cvt_pk_f16_f32 v235, v226, v227
	v_pk_max_f16 v234, v234, 0
	v_pk_max_f16 v235, v235, 0
	v_mfma_f32_16x16x32_f16 v[160:163], v[220:223], v[196:199], v[160:163]
	v_cvt_pk_f16_f32 v190, v204, v205
	v_cvt_pk_f16_f32 v191, v206, v207
	v_pk_max_f16 v190, v190, 0
	v_pk_max_f16 v191, v191, 0
	v_mfma_f32_16x16x32_f16 v[192:195], v[240:243], v[180:183], 0
	v_cvt_pk_f16_f32 v236, v228, v229
	v_cvt_pk_f16_f32 v237, v230, v231
	v_pk_max_f16 v236, v236, 0
	v_pk_max_f16 v237, v237, 0
	v_mfma_f32_16x16x32_f16 v[192:195], v[244:247], v[188:191], v[192:195]
	v_cvt_pk_f16_f32 v238, v216, v217
	v_cvt_pk_f16_f32 v239, v218, v219
	v_pk_max_f16 v238, v238, 0
	v_pk_max_f16 v239, v239, 0
	v_cvt_pk_f16_f32 v180, v200, v201
	v_cvt_pk_f16_f32 v181, v202, v203
	v_pk_max_f16 v180, v180, 0
	v_pk_max_f16 v181, v181, 0
	v_mfma_f32_16x16x32_f16 v[196:199], v[240:243], v[232:235], 0
	v_cvt_pk_f16_f32 v182, v136, v137
	v_cvt_pk_f16_f32 v183, v138, v139
	v_pk_max_f16 v182, v182, 0
	v_pk_max_f16 v183, v183, 0
	v_mfma_f32_16x16x32_f16 v[196:199], v[244:247], v[236:239], v[196:199]
	v_cvt_pk_f16_f32 v188, v184, v185
	v_cvt_pk_f16_f32 v189, v186, v187
	v_pk_max_f16 v188, v188, 0
	v_pk_max_f16 v189, v189, 0
	v_cvt_pk_f16_f32 v190, v160, v161
	v_cvt_pk_f16_f32 v191, v162, v163
	v_pk_max_f16 v190, v190, 0
	v_pk_max_f16 v191, v191, 0
	v_mfma_f32_16x16x32_f16 v[122:125], v[240:243], v[180:183], 0
	s_nop 0
	v_mfma_f32_16x16x32_f16 v[122:125], v[244:247], v[188:191], v[122:125]
	v_add_u32_e32 v145, 0x12c00, v105
	v_cndmask_b32_e64 v0, v252, v192, s[2:3]
	v_cndmask_b32_e64 v0, v0, v196, s[0:1]
	s_waitcnt vmcnt(16)
	v_cndmask_b32_e64 v1, v30, v134, s[0:1]
	v_bfi_b32 v30, s10, v1, v30
	v_perm_b32 v1, v22, v134, s24
	v_cndmask_b32_e64 v22, v22, v1, s[0:1]
	v_cndmask_b32_e64 v0, v0, v122, s[26:27]
	ds_write_b32 v112, v0
	v_bfi_b32 v1, s10, v135, v18
	v_perm_b32 v121, v10, v135, s24
	v_cndmask_b32_e64 v18, v18, v1, s[0:1]
	v_cndmask_b32_e64 v10, v10, v121, s[0:1]
	s_add_i32 s22, s22, 0x80000
	s_add_i32 s11, s11, 1
	s_add_u32 s12, s12, 4
	s_addc_u32 s13, s13, 0
	v_add_u32_e32 v104, 0x400, v104
	v_add_u32_e32 v105, 0x800, v105
	v_add_u32_e32 v114, 2, v114
	s_cmp_eq_u32 s22, 0x898000
	s_waitcnt lgkmcnt(0)
	s_barrier
	ds_read_b128 v[232:235], v113
	ds_read_b128 v[236:239], v113 offset:1024
	ds_read_b128 v[240:243], v145 offset:2048
	ds_read_b128 v[244:247], v145 offset:2064
	ds_read_b128 v[248:251], v145 offset:2080
	ds_read_b128 v[252:255], v145 offset:2096
	s_waitcnt lgkmcnt(4)
	v_add_f32_e32 v0, v232, v233
	v_add_f32_e32 v1, v234, v235
	v_add_f32_e32 v121, v236, v237
	v_add_f32_e32 v144, v238, v239
	v_add_f32_e32 v0, v0, v1
	v_add_f32_e32 v121, v121, v144
	v_add_f32_e32 v0, v0, v121
	v_add_f32_e32 v0, s30, v0
	v_cvt_f16_f32_e32 v1, v0
	v_cvt_f16_f32_e32 v121, v0
	ds_write_b32 v106, v0
	v_add_u32_e32 v106, 4, v106
	v_permlane16_swap_b32_e32 v1, v121
	s_cbranch_scc0 .LBB1_4
